# speedup vs baseline: 1.0077x; 1.0077x over previous
.Lstag_done_p1:
	s_lshr_b32 s22, s2, 3
	s_sub_i32 s22, 0xbf, s22
	s_and_b32 s2, s2, 7
	s_lshl_b32 s22, s22, 3
	s_or_b32 s2, s2, s22
	s_ashr_i32 s15, s2, 3
	s_mul_hi_i32 s14, s15, 0x55555556
	s_lshr_b32 s12, s14, 31
	s_add_i32 s14, s14, s12
	s_mul_i32 s16, s14, 0x3fffffd
	s_add_i32 s16, s16, s15
	s_lshl_b32 s15, s16, 6
	s_lshl_b32 s16, s2, 5
	s_and_b32 s16, s16, 32
	s_or_b32 s15, s15, s16
	s_bfe_u32 s16, s2, 0x20001
	s_mul_i32 s2, s16, 0xc0
	s_lshl_b32 s12, s14, 1
	s_add_i32 s17, s15, s2
	s_load_dwordx8 s[4:11], s[0:1], 0x0
	s_and_b32 s12, s12, -16
	s_lshl_b32 s13, s14, 4
	s_and_b32 s13, s13, 0x70
	s_mov_b32 s3, 0
	v_mov_b32_e32 v32, 0
	v_lshrrev_b32_e32 v78, 6, v0
	v_bfe_u32 v65, v0, 2, 4
	v_lshlrev_b32_e32 v1, 4, v0
	v_and_b32_e32 v30, 48, v1
	v_lshl_add_u32 v1, v78, 7, v65
	v_lshl_add_u32 v1, v1, 9, v30
	s_lshl_b32 s18, s17, 7
	s_add_i32 s18, s18, s12
	s_lshl_b32 s18, s18, 9
	s_lshl_b32 s2, s13, 2
	s_add_i32 s18, s18, s2
	s_waitcnt lgkmcnt(0)
	s_add_u32 s20, s4, s18
	s_addc_u32 s21, s5, 0
	s_add_u32 s22, s20, 0x40000
	s_addc_u32 s23, s21, 0
	s_add_u32 s24, s22, 0x40000
	s_addc_u32 s25, s23, 0
	s_add_u32 s26, s24, 0x40000
	s_addc_u32 s27, s25, 0
	s_add_u32 s28, s26, 0x40000
	s_addc_u32 s29, s27, 0
	s_add_u32 s30, s28, 0x40000
	s_addc_u32 s31, s29, 0
	s_add_u32 s32, s30, 0x40000
	s_addc_u32 s33, s31, 0
	s_add_u32 s34, s32, 0x40000
	s_addc_u32 s35, s33, 0
	v_readfirstlane_b32 s19, v78
	s_nop 3
	s_mul_i32 s19, s19, 0x410
	s_add_i32 m0, s19, 29120
	s_nop 0
	global_load_lds_dwordx4 v1, s[34:35]
	s_add_i32 m0, s19, 24960
	s_nop 0
	global_load_lds_dwordx4 v1, s[32:33]
	s_add_i32 m0, s19, 20800
	s_nop 0
	global_load_lds_dwordx4 v1, s[30:31]
	s_add_i32 m0, s19, 16640
	s_nop 0
	global_load_lds_dwordx4 v1, s[28:29]
	s_add_i32 m0, s19, 12480
	s_nop 0
	global_load_lds_dwordx4 v1, s[26:27]
	s_add_i32 m0, s19, 8320
	s_nop 0
	global_load_lds_dwordx4 v1, s[24:25]
	v_bfe_u32 v103, v0, 5, 1
	v_lshrrev_b32_e32 v33, 2, v0
	s_add_i32 m0, s19, 4160
	s_nop 0
	global_load_lds_dwordx4 v1, s[22:23]
	s_mov_b32 m0, s19
	s_nop 0
	global_load_lds_dwordx4 v1, s[20:21]
	v_lshlrev_b32_e32 v104, 1, v78
	v_and_b32_e32 v27, 3, v0
	v_lshrrev_b32_e32 v28, 1, v0
	v_and_or_b32 v59, v33, 1, v104
	v_and_or_b32 v105, v28, 12, v27
	v_lshlrev_b32_e32 v28, 4, v103
	v_mov_b32_e32 v29, v32
	v_lshl_add_u64 v[56:57], s[6:7], 0, v[28:29]
	v_or_b32_e32 v27, s13, v59
	v_or_b32_e32 v28, s12, v105
	s_lshl_b32 s4, s16, 16
	v_lshl_add_u32 v31, v27, 7, v28
	s_or_b32 s2, s4, 0x4000
	v_add_u32_e32 v27, 0x400, v31
	s_or_b32 s5, s4, 0xc000
	v_add_u32_e32 v28, s2, v27
	v_and_b32_e32 v1, 31, v0
	v_ashrrev_i32_e32 v29, 31, v28
	v_add_u32_e32 v34, s5, v27
	v_or_b32_e32 v26, s15, v1
	v_lshlrev_b64 v[28:29], 5, v[28:29]
	v_ashrrev_i32_e32 v35, 31, v34
	v_lshl_add_u64 v[28:29], v[56:57], 0, v[28:29]
	v_lshlrev_b64 v[34:35], 5, v[34:35]
	v_lshl_or_b32 v58, v26, 1, v103
	v_lshl_add_u64 v[34:35], v[56:57], 0, v[34:35]
	global_load_dwordx4 v[36:39], v[28:29], off
	global_load_dwordx4 v[40:43], v[34:35], off
	v_add_u32_e32 v28, 0x180, v58
	v_ashrrev_i32_e32 v29, 31, v28
	v_add_u32_e32 v34, 0x480, v58
	v_lshl_add_u64 v[28:29], v[28:29], 4, s[8:9]
	v_ashrrev_i32_e32 v35, 31, v34
	v_ashrrev_i32_e32 v27, 31, v26
	v_lshl_add_u64 v[34:35], v[34:35], 4, s[8:9]
	global_load_dwordx4 v[44:47], v[28:29], off
	global_load_dwordx4 v[48:51], v[34:35], off
	v_lshl_add_u64 v[60:61], v[26:27], 2, s[10:11]
	v_add_u32_e32 v26, s5, v31
	v_add_u32_e32 v28, s2, v31
	v_ashrrev_i32_e32 v27, 31, v26
	v_ashrrev_i32_e32 v29, 31, v28
	v_lshlrev_b64 v[26:27], 5, v[26:27]
	v_lshlrev_b64 v[28:29], 5, v[28:29]
	global_load_dword v62, v[60:61], off offset:768
	global_load_dword v64, v[60:61], off offset:2304
	v_lshl_add_u64 v[26:27], v[56:57], 0, v[26:27]
	v_lshl_add_u64 v[28:29], v[56:57], 0, v[28:29]
	global_load_dwordx4 v[52:55], v[26:27], off
	s_nop 0
	global_load_dwordx4 v[26:29], v[28:29], off
	s_load_dwordx2 s[0:1], s[0:1], 0x28
	v_and_b32_e32 v0, 63, v0
	v_bfrev_b32_e32 v31, 60
	v_cmp_gt_u32_e32 vcc, 32, v0
	v_mul_u32_u24_e32 v102, 0x410, v1
	v_lshlrev_b32_e32 v0, 2, v1
	v_mov_b32_e32 v1, v32
	v_cndmask_b32_e64 v34, v31, 0, vcc
	s_waitcnt lgkmcnt(0)
	v_lshl_add_u64 v[72:73], s[0:1], 0, v[0:1]
	s_mov_b64 s[36:37], s[0:1]
	v_mov_b32_e32 v110, v0
	v_mul_u32_u24_e32 v0, 0x410, v78
	v_lshlrev_b32_e32 v1, 6, v65
	v_add3_u32 v1, v0, v1, v30
	s_mul_i32 s16, s16, 24
	s_lshr_b32 s0, s15, 5
	s_waitcnt vmcnt(8)
	s_add_i32 s0, s0, s16
	s_waitcnt lgkmcnt(0)
	s_barrier
	s_lshl_b32 s2, s0, 10
	v_mov_b32_e32 v33, v32
	v_mov_b32_e32 v35, v32
	v_lshl_or_b32 v106, v103, 2, v102
	s_add_i32 s5, s2, 0x4800
	v_or_b32_e32 v107, s13, v103
	s_ashr_i32 s6, s14, 3
	s_add_i32 s7, s2, 0x1800
	s_mov_b64 s[0:1], -1
	s_mov_b32 s10, 0x7f61b1e6
	s_mov_b32 s11, 0x42800000
	s_waitcnt vmcnt(3)
	v_mov_b32_e32 v63, v62
	s_waitcnt vmcnt(2)
	v_mov_b32_e32 v65, v64
	s_waitcnt vmcnt(0)
	s_branch .LBB2_3
.LBB2_2:
	v_add_f32_e32 v1, v66, v67
	v_add_u32_e32 v0, v107, v108
	v_mul_f32_e32 v1, v62, v1
	v_lshl_add_u32 v2, v0, 3, s6
	v_exp_f32_e32 v4, v1
	v_mul_f32_e32 v5, v64, v82
	v_add_u32_e32 v0, s5, v2
	v_add_u32_e32 v2, s7, v2
	v_exp_f32_e32 v5, v5
	v_lshl_add_u32 v2, v2, 7, v110
	s_xor_b64 s[14:15], s[0:1], -1
	v_cvt_pk_f16_f32 v4, v4, v71
	v_lshl_add_u32 v0, v0, 7, v110
	v_mov_b64_e32 v[54:55], v[42:43]
	v_mov_b64_e32 v[26:27], v[36:37]
	global_store_dword v2, v4, s[36:37]
	v_cvt_pk_f16_f32 v2, v5, v83
	s_mov_b32 s3, 8
	s_mov_b64 s[0:1], 0
	s_andn2_b64 vcc, exec, s[14:15]
	v_mov_b64_e32 v[52:53], v[40:41]
	v_mov_b64_e32 v[28:29], v[38:39]
	global_store_dword v0, v2, s[36:37]
	s_cbranch_vccz .LBB2_8

.LBB2_9:
	v_add_f32_e32 v1, v78, v79
	v_add_u32_e32 v0, s12, v97
	v_mul_f32_e32 v1, v74, v1
	v_lshl_or_b32 v2, v0, 3, s4
	v_exp_f32_e32 v4, v1
	v_mul_f32_e32 v5, v76, v66
	v_add_u32_e32 v0, s3, v2
	v_add_u32_e32 v2, s2, v2
	v_exp_f32_e32 v5, v5
	v_lshl_add_u32 v2, v2, 7, v110
	s_xor_b64 s[8:9], s[0:1], -1
	v_cvt_pk_f16_f32 v4, v4, v81
	v_lshl_add_u32 v0, v0, 7, v110
	v_mov_b64_e32 v[58:59], v[42:43]
	v_mov_b64_e32 v[16:17], v[36:37]
	global_store_dword v2, v4, s[36:37]
	v_cvt_pk_f16_f32 v2, v5, v67
	s_mov_b32 s7, 8
	s_mov_b64 s[0:1], 0
	s_andn2_b64 vcc, exec, s[8:9]
	v_mov_b64_e32 v[56:57], v[40:41]
	v_mov_b64_e32 v[18:19], v[38:39]
	global_store_dword v0, v2, s[36:37]
	s_cbranch_vccz .LBB2_15

	.amdhsa_kernel _Z11scan_kernelILi1ELi1536ELi4EEvPKfPKDF16_S3_S1_S1_PDv2_DF16_S3_Pf
		.amdhsa_group_segment_fixed_size 33280
		.amdhsa_private_segment_fixed_size 0
		.amdhsa_kernarg_size 64
		.amdhsa_user_sgpr_count 2
		.amdhsa_user_sgpr_dispatch_ptr 0
		.amdhsa_user_sgpr_queue_ptr 0
		.amdhsa_user_sgpr_kernarg_segment_ptr 1
		.amdhsa_user_sgpr_dispatch_id 0
		.amdhsa_user_sgpr_kernarg_preload_length 0
		.amdhsa_user_sgpr_kernarg_preload_offset 0
		.amdhsa_user_sgpr_private_segment_size 0
		.amdhsa_uses_dynamic_stack 0
		.amdhsa_enable_private_segment 0
		.amdhsa_system_sgpr_workgroup_id_x 1
		.amdhsa_system_sgpr_workgroup_id_y 0
		.amdhsa_system_sgpr_workgroup_id_z 0
		.amdhsa_system_sgpr_workgroup_info 0
		.amdhsa_system_vgpr_workitem_id 0
		.amdhsa_next_free_vgpr 111
		.amdhsa_next_free_sgpr 96
		.amdhsa_accum_offset 112
		.amdhsa_reserve_vcc 1
		.amdhsa_float_round_mode_32 0
		.amdhsa_float_round_mode_16_64 0
		.amdhsa_float_denorm_mode_32 3
		.amdhsa_float_denorm_mode_16_64 3
		.amdhsa_dx10_clamp 1
		.amdhsa_ieee_mode 1
		.amdhsa_fp16_overflow 0
		.amdhsa_tg_split 0
		.amdhsa_exception_fp_ieee_invalid_op 0
		.amdhsa_exception_fp_denorm_src 0
		.amdhsa_exception_fp_ieee_div_zero 0
		.amdhsa_exception_fp_ieee_overflow 0
		.amdhsa_exception_fp_ieee_underflow 0
		.amdhsa_exception_fp_ieee_inexact 0
		.amdhsa_exception_int_div_zero 0
	.end_amdhsa_kernel

amdhsa.kernels:
  - .agpr_count:     0
    .args:
      - .actual_access:  read_only
        .address_space:  global
        .offset:         0
        .size:           8
        .value_kind:     global_buffer
      - .actual_access:  read_only
        .address_space:  global
        .offset:         8
        .size:           8
        .value_kind:     global_buffer
      - .actual_access:  read_only
        .address_space:  global
        .offset:         16
        .size:           8
        .value_kind:     global_buffer
      - .actual_access:  read_only
        .address_space:  global
        .offset:         24
        .size:           8
        .value_kind:     global_buffer
      - .actual_access:  read_only
        .address_space:  global
        .offset:         32
        .size:           8
        .value_kind:     global_buffer
      - .actual_access:  read_only
        .address_space:  global
        .offset:         40
        .size:           8
        .value_kind:     global_buffer
      - .actual_access:  write_only
        .address_space:  global
        .offset:         48
        .size:           8
        .value_kind:     global_buffer
      - .actual_access:  write_only
        .address_space:  global
        .offset:         56
        .size:           8
        .value_kind:     global_buffer
      - .actual_access:  write_only
        .address_space:  global
        .offset:         64
        .size:           8
        .value_kind:     global_buffer
      - .actual_access:  write_only
        .address_space:  global
        .offset:         72
        .size:           8
        .value_kind:     global_buffer
    .group_segment_fixed_size: 65536
    .kernarg_segment_align: 8
    .kernarg_segment_size: 80
    .language:       OpenCL C
    .language_version:
      - 2
      - 0
    .max_flat_workgroup_size: 256
    .name:           _Z11proj_kernelPKfS0_S0_S0_S0_S0_PDF16_S1_PfS2_
    .private_segment_fixed_size: 0
    .sgpr_count:     22
    .sgpr_spill_count: 0
    .symbol:         _Z11proj_kernelPKfS0_S0_S0_S0_S0_PDF16_S1_PfS2_.kd
    .uniform_work_group_size: 1
    .uses_dynamic_stack: false
    .vgpr_count:     200
    .vgpr_spill_count: 0
    .wavefront_size: 64
  - .agpr_count:     0
    .args:
      - .actual_access:  read_only
        .address_space:  global
        .offset:         0
        .size:           8
        .value_kind:     global_buffer
      - .actual_access:  write_only
        .address_space:  global
        .offset:         8
        .size:           8
        .value_kind:     global_buffer
    .group_segment_fixed_size: 12672
    .kernarg_segment_align: 8
    .kernarg_segment_size: 16
    .language:       OpenCL C
    .language_version:
      - 2
      - 0
    .max_flat_workgroup_size: 1024
    .name:           _Z12carry_kernelPKDv2_DF16_PDF16_
    .private_segment_fixed_size: 0
    .sgpr_count:     16
    .sgpr_spill_count: 0
    .symbol:         _Z12carry_kernelPKDv2_DF16_PDF16_.kd
    .uniform_work_group_size: 1
    .uses_dynamic_stack: false
    .vgpr_count:     92
    .vgpr_spill_count: 0
    .wavefront_size: 64
  - .agpr_count:     0
    .args:
      - .actual_access:  read_only
        .address_space:  global
        .offset:         0
        .size:           8
        .value_kind:     global_buffer
      - .actual_access:  read_only
        .address_space:  global
        .offset:         8
        .size:           8
        .value_kind:     global_buffer
      - .actual_access:  read_only
        .address_space:  global
        .offset:         16
        .size:           8
        .value_kind:     global_buffer
      - .actual_access:  read_only
        .address_space:  global
        .offset:         24
        .size:           8
        .value_kind:     global_buffer
      - .actual_access:  read_only
        .address_space:  global
        .offset:         32
        .size:           8
        .value_kind:     global_buffer
      - .actual_access:  write_only
        .address_space:  global
        .offset:         40
        .size:           8
        .value_kind:     global_buffer
      - .actual_access:  read_only
        .address_space:  global
        .offset:         48
        .size:           8
        .value_kind:     global_buffer
      - .actual_access:  read_only
        .address_space:  global
        .offset:         56
        .size:           8
        .value_kind:     global_buffer
    .group_segment_fixed_size: 33280
    .kernarg_segment_align: 8
    .kernarg_segment_size: 64
    .language:       OpenCL C
    .language_version:
      - 2
      - 0
    .max_flat_workgroup_size: 256
    .name:           _Z11scan_kernelILi1ELi1536ELi4EEvPKfPKDF16_S3_S1_S1_PDv2_DF16_S3_Pf
    .private_segment_fixed_size: 0
    .sgpr_count:     24
    .sgpr_spill_count: 0
    .symbol:         _Z11scan_kernelILi1ELi1536ELi4EEvPKfPKDF16_S3_S1_S1_PDv2_DF16_S3_Pf.kd
    .uniform_work_group_size: 1
    .uses_dynamic_stack: false
    .vgpr_count:     111
    .vgpr_spill_count: 0
    .wavefront_size: 64
  - .agpr_count:     0
    .args:
      - .actual_access:  read_only
        .address_space:  global
        .offset:         0
        .size:           8
        .value_kind:     global_buffer
      - .actual_access:  read_only
        .address_space:  global
        .offset:         8
        .size:           8
        .value_kind:     global_buffer
      - .actual_access:  read_only
        .address_space:  global
        .offset:         16
        .size:           8
        .value_kind:     global_buffer
      - .actual_access:  read_only
        .address_space:  global
        .offset:         24
        .size:           8
        .value_kind:     global_buffer
      - .actual_access:  read_only
        .address_space:  global
        .offset:         32
        .size:           8
        .value_kind:     global_buffer
      - .actual_access:  read_only
        .address_space:  global
        .offset:         40
        .size:           8
        .value_kind:     global_buffer
      - .actual_access:  read_only
        .address_space:  global
        .offset:         48
        .size:           8
        .value_kind:     global_buffer
      - .actual_access:  write_only
        .address_space:  global
        .offset:         56
        .size:           8
        .value_kind:     global_buffer
    .group_segment_fixed_size: 50176
    .kernarg_segment_align: 8
    .kernarg_segment_size: 64
    .language:       OpenCL C
    .language_version:
      - 2
      - 0
    .max_flat_workgroup_size: 256
    .name:           _Z11scan_kernelILi3ELi1536ELi3EEvPKfPKDF16_S3_S1_S1_PDv2_DF16_S3_Pf
    .private_segment_fixed_size: 0
    .sgpr_count:     28
    .sgpr_spill_count: 0
    .symbol:         _Z11scan_kernelILi3ELi1536ELi3EEvPKfPKDF16_S3_S1_S1_PDv2_DF16_S3_Pf.kd
    .uniform_work_group_size: 1
    .uses_dynamic_stack: false
    .vgpr_count:     168
    .vgpr_spill_count: 0
    .wavefront_size: 64
